# GQA tile loops: the ten K-fragment and eight V-fragment LDS reads of a tile issued ahead into free register quads (counted waits) instead of read-wait-MFMA chains
# speedup vs baseline: 1.0074x; 1.0038x over previous
.LBB0_763:
	ds_read_b128 v[178:181], v131 offset:9216
	ds_read_b128 v[182:185], v131 offset:9248
	ds_read_b128 v[186:189], v131 offset:13824
	ds_read_b128 v[190:193], v131 offset:13856
	ds_read_b128 v[194:197], v131 offset:9280
	ds_read_b128 v[198:201], v131 offset:13888
	ds_read_b128 v[202:205], v131 offset:9312
	ds_read_b128 v[206:209], v131 offset:13920
	v_exp_f32_e32 v38, v38
	v_exp_f32_e32 v39, v39
	v_exp_f32_e32 v54, v54
	v_exp_f32_e32 v55, v55
	v_exp_f32_e32 v40, v40
	v_exp_f32_e32 v41, v41
	v_exp_f32_e32 v56, v56
	v_exp_f32_e32 v57, v57
	v_exp_f32_e32 v42, v42
	v_exp_f32_e32 v43, v43
	v_exp_f32_e32 v142, v50
	v_exp_f32_e32 v143, v51
	v_pk_add_f32 v[50:51], v[126:127], v[38:39]
	v_exp_f32_e32 v58, v58
	v_exp_f32_e32 v59, v59
	v_pk_add_f32 v[50:51], v[54:55], v[50:51]
	v_exp_f32_e32 v44, v44
	v_exp_f32_e32 v45, v45
	v_pk_add_f32 v[50:51], v[40:41], v[50:51]
	v_exp_f32_e32 v60, v60
	v_exp_f32_e32 v61, v61
	v_pk_add_f32 v[50:51], v[56:57], v[50:51]
	v_exp_f32_e32 v46, v46
	v_exp_f32_e32 v47, v47
	v_pk_add_f32 v[50:51], v[42:43], v[50:51]
	v_exp_f32_e32 v62, v62
	v_exp_f32_e32 v63, v63
	v_pk_add_f32 v[50:51], v[58:59], v[50:51]
	v_exp_f32_e32 v48, v48
	v_exp_f32_e32 v49, v49
	v_pk_add_f32 v[50:51], v[44:45], v[50:51]
	v_exp_f32_e32 v64, v64
	v_exp_f32_e32 v65, v65
	v_pk_add_f32 v[50:51], v[60:61], v[50:51]
	v_exp_f32_e32 v66, v66
	v_pk_add_f32 v[50:51], v[46:47], v[50:51]
	v_exp_f32_e32 v67, v67
	v_pk_add_f32 v[50:51], v[62:63], v[50:51]
	v_exp_f32_e32 v144, v52
	v_exp_f32_e32 v145, v53
	v_pk_add_f32 v[50:51], v[48:49], v[50:51]
	v_exp_f32_e32 v68, v68
	v_exp_f32_e32 v69, v69
	v_pk_add_f32 v[50:51], v[64:65], v[50:51]
	v_cvt_pk_bf16_f32 v52, v42, v43
	v_pk_add_f32 v[50:51], v[142:143], v[50:51]
	v_cvt_pk_bf16_f32 v53, v44, v45
	v_cvt_pk_bf16_f32 v42, v54, v55
	v_cvt_pk_bf16_f32 v43, v56, v57
	v_cvt_pk_bf16_f32 v44, v58, v59
	v_cvt_pk_bf16_f32 v45, v60, v61
	v_pk_add_f32 v[50:51], v[66:67], v[50:51]
	v_cvt_pk_bf16_f32 v46, v46, v47
	v_pk_add_f32 v[50:51], v[144:145], v[50:51]
	v_cvt_pk_bf16_f32 v47, v48, v49
	v_pk_add_f32 v[126:127], v[68:69], v[50:51]
	v_cvt_pk_bf16_f32 v50, v38, v39
	v_cvt_pk_bf16_f32 v51, v40, v41
	v_cvt_pk_bf16_f32 v48, v142, v143
	v_cvt_pk_bf16_f32 v49, v144, v145
	s_waitcnt lgkmcnt(0)
	v_mfma_f32_32x32x16_bf16 v[6:21], v[178:181], v[50:53], v[6:21]
	v_cvt_pk_bf16_f32 v38, v62, v63
	v_cvt_pk_bf16_f32 v39, v64, v65
	v_cvt_pk_bf16_f32 v40, v66, v67
	v_cvt_pk_bf16_f32 v41, v68, v69
	s_addk_i32 s39, 0x4800
	s_cmp_eq_u32 s39, 0x12000
	v_mfma_f32_32x32x16_bf16 v[22:37], v[186:189], v[50:53], v[22:37]
	v_mfma_f32_32x32x16_bf16 v[6:21], v[182:185], v[46:49], v[6:21]
	v_mfma_f32_32x32x16_bf16 v[22:37], v[190:193], v[46:49], v[22:37]
	v_mfma_f32_32x32x16_bf16 v[6:21], v[194:197], v[42:45], v[6:21]
	v_mfma_f32_32x32x16_bf16 v[22:37], v[198:201], v[42:45], v[22:37]
	v_mfma_f32_32x32x16_bf16 v[6:21], v[202:205], v[38:41], v[6:21]
	v_mfma_f32_32x32x16_bf16 v[22:37], v[206:209], v[38:41], v[22:37]
	s_cbranch_scc1 .LBB0_827
.LBB0_764:
	v_add_u32_e32 v131, s39, v1
	ds_read_b128 v[38:41], v131
	ds_read_b128 v[142:145], v131 offset:32
	ds_read_b128 v[54:57], v131 offset:4608
	ds_read_b128 v[148:151], v131 offset:4640
	ds_read_b128 v[152:155], v131 offset:64
	ds_read_b128 v[156:159], v131 offset:4672
	ds_read_b128 v[160:163], v131 offset:96
	ds_read_b128 v[164:167], v131 offset:4704
	ds_read_b128 v[168:171], v131 offset:128
	ds_read_b128 v[172:175], v131 offset:4736
	s_waitcnt lgkmcnt(9)
	v_mfma_f32_32x32x16_bf16 v[38:53], v[38:41], v[82:85], 0
	s_waitcnt lgkmcnt(8)
	v_mfma_f32_32x32x16_bf16 v[38:53], v[142:145], v[78:81], v[38:53]
	s_waitcnt lgkmcnt(7)
	v_mfma_f32_32x32x16_bf16 v[54:69], v[54:57], v[82:85], 0
	s_waitcnt lgkmcnt(6)
	v_mfma_f32_32x32x16_bf16 v[54:69], v[148:151], v[78:81], v[54:69]
	s_waitcnt lgkmcnt(5)
	v_mfma_f32_32x32x16_bf16 v[38:53], v[152:155], v[74:77], v[38:53]
	s_waitcnt lgkmcnt(4)
	v_mfma_f32_32x32x16_bf16 v[54:69], v[156:159], v[74:77], v[54:69]
	s_waitcnt lgkmcnt(3)
	v_mfma_f32_32x32x16_bf16 v[38:53], v[160:163], v[70:73], v[38:53]
	s_waitcnt lgkmcnt(2)
	v_mfma_f32_32x32x16_bf16 v[54:69], v[164:167], v[70:73], v[54:69]
	s_waitcnt lgkmcnt(1)
	v_mfma_f32_32x32x16_bf16 v[38:53], v[168:171], v[86:89], v[38:53]
	s_waitcnt lgkmcnt(0)
	v_mfma_f32_32x32x16_bf16 v[54:69], v[172:175], v[86:89], v[54:69]
	s_nop 11
	v_max_i32_e32 v2, v38, v54
	v_max3_i32 v2, v2, v39, v55
	v_max3_i32 v2, v2, v40, v56
	v_max3_i32 v2, v2, v41, v57
	v_max3_i32 v2, v2, v42, v58
	v_max3_i32 v2, v2, v43, v59
	v_max3_i32 v2, v2, v44, v60
	v_max3_i32 v2, v2, v45, v61
	v_max3_i32 v2, v2, v46, v62
	v_max3_i32 v2, v2, v47, v63
	v_max3_i32 v2, v2, v48, v64
	v_max3_i32 v2, v2, v49, v65
	v_max3_i32 v2, v2, v50, v66
	v_max3_i32 v2, v2, v51, v67
	v_max3_i32 v2, v2, v52, v68
	v_max3_i32 v2, v2, v53, v69
	v_mov_b32_e32 v5, v2
	s_nop 1
	v_permlane32_swap_b32_e32 v2, v5
	v_max_i32_e32 v2, v2, v5
	v_cmp_lt_f32_e32 vcc, s29, v2
	s_cbranch_vccz .LBB0_763
	v_mov_b32_e32 v141, v4
	s_and_saveexec_b64 s[10:11], vcc
	s_cbranch_execz .LBB0_762
	v_add_f32_e32 v2, v4, v2
	v_cvt_pk_bf16_f32 v2, v2, 0
	v_lshlrev_b32_e32 v141, 16, v2
	s_branch .LBB0_762

.LBB0_771:
	ds_read_b128 v[178:181], v94 offset:9216
	ds_read_b128 v[182:185], v94 offset:9248
	ds_read_b128 v[186:189], v94 offset:13824
	ds_read_b128 v[190:193], v94 offset:13856
	ds_read_b128 v[194:197], v94 offset:9280
	ds_read_b128 v[198:201], v94 offset:13888
	ds_read_b128 v[202:205], v94 offset:9312
	ds_read_b128 v[206:209], v94 offset:13920
	v_exp_f32_e32 v38, v38
	v_exp_f32_e32 v39, v39
	v_exp_f32_e32 v54, v54
	v_exp_f32_e32 v55, v55
	v_exp_f32_e32 v40, v40
	v_exp_f32_e32 v41, v41
	v_exp_f32_e32 v56, v56
	v_exp_f32_e32 v57, v57
	v_exp_f32_e32 v42, v42
	v_exp_f32_e32 v43, v43
	v_exp_f32_e32 v96, v50
	v_exp_f32_e32 v97, v51
	v_pk_add_f32 v[50:51], v[132:133], v[38:39]
	v_exp_f32_e32 v58, v58
	v_exp_f32_e32 v59, v59
	v_pk_add_f32 v[50:51], v[54:55], v[50:51]
	v_exp_f32_e32 v44, v44
	v_exp_f32_e32 v45, v45
	v_pk_add_f32 v[50:51], v[40:41], v[50:51]
	v_exp_f32_e32 v60, v60
	v_exp_f32_e32 v61, v61
	v_pk_add_f32 v[50:51], v[56:57], v[50:51]
	v_exp_f32_e32 v46, v46
	v_exp_f32_e32 v47, v47
	v_pk_add_f32 v[50:51], v[42:43], v[50:51]
	v_exp_f32_e32 v62, v62
	v_exp_f32_e32 v63, v63
	v_pk_add_f32 v[50:51], v[58:59], v[50:51]
	v_exp_f32_e32 v48, v48
	v_exp_f32_e32 v49, v49
	v_pk_add_f32 v[50:51], v[44:45], v[50:51]
	v_exp_f32_e32 v64, v64
	v_exp_f32_e32 v65, v65
	v_pk_add_f32 v[50:51], v[60:61], v[50:51]
	v_exp_f32_e32 v66, v66
	v_pk_add_f32 v[50:51], v[46:47], v[50:51]
	v_exp_f32_e32 v67, v67
	v_pk_add_f32 v[50:51], v[62:63], v[50:51]
	v_exp_f32_e32 v144, v52
	v_exp_f32_e32 v145, v53
	v_pk_add_f32 v[50:51], v[48:49], v[50:51]
	v_exp_f32_e32 v68, v68
	v_exp_f32_e32 v69, v69
	v_pk_add_f32 v[50:51], v[64:65], v[50:51]
	v_cvt_pk_bf16_f32 v52, v42, v43
	v_pk_add_f32 v[50:51], v[96:97], v[50:51]
	v_cvt_pk_bf16_f32 v53, v44, v45
	v_cvt_pk_bf16_f32 v42, v54, v55
	v_cvt_pk_bf16_f32 v43, v56, v57
	v_cvt_pk_bf16_f32 v44, v58, v59
	v_cvt_pk_bf16_f32 v45, v60, v61
	v_pk_add_f32 v[50:51], v[66:67], v[50:51]
	v_cvt_pk_bf16_f32 v46, v46, v47
	v_pk_add_f32 v[50:51], v[144:145], v[50:51]
	v_cvt_pk_bf16_f32 v47, v48, v49
	v_pk_add_f32 v[132:133], v[68:69], v[50:51]
	v_cvt_pk_bf16_f32 v50, v38, v39
	v_cvt_pk_bf16_f32 v51, v40, v41
	v_cvt_pk_bf16_f32 v48, v96, v97
	v_cvt_pk_bf16_f32 v49, v144, v145
	s_waitcnt lgkmcnt(0)
	v_mfma_f32_32x32x16_bf16 v[6:21], v[178:181], v[50:53], v[6:21]
	v_cvt_pk_bf16_f32 v38, v62, v63
	v_cvt_pk_bf16_f32 v39, v64, v65
	v_cvt_pk_bf16_f32 v40, v66, v67
	v_cvt_pk_bf16_f32 v41, v68, v69
	s_addk_i32 s12, 0x4800
	s_cmp_lg_u32 s12, 0x12000
	v_mfma_f32_32x32x16_bf16 v[22:37], v[186:189], v[50:53], v[22:37]
	v_mfma_f32_32x32x16_bf16 v[6:21], v[182:185], v[46:49], v[6:21]
	v_mfma_f32_32x32x16_bf16 v[22:37], v[190:193], v[46:49], v[22:37]
	v_mfma_f32_32x32x16_bf16 v[6:21], v[194:197], v[42:45], v[6:21]
	v_mfma_f32_32x32x16_bf16 v[22:37], v[198:201], v[42:45], v[22:37]
	v_mfma_f32_32x32x16_bf16 v[6:21], v[202:205], v[38:41], v[6:21]
	v_mfma_f32_32x32x16_bf16 v[22:37], v[206:209], v[38:41], v[22:37]
	s_cbranch_scc0 .LBB0_775
.LBB0_772:
	v_add_u32_e32 v94, s12, v1
	ds_read_b128 v[38:41], v94
	ds_read_b128 v[144:147], v94 offset:32
	ds_read_b128 v[54:57], v94 offset:4608
	ds_read_b128 v[148:151], v94 offset:4640
	ds_read_b128 v[152:155], v94 offset:64
	ds_read_b128 v[156:159], v94 offset:4672
	ds_read_b128 v[160:163], v94 offset:96
	ds_read_b128 v[164:167], v94 offset:4704
	ds_read_b128 v[168:171], v94 offset:128
	ds_read_b128 v[172:175], v94 offset:4736
	s_waitcnt lgkmcnt(9)
	v_mfma_f32_32x32x16_bf16 v[38:53], v[38:41], v[82:85], 0
	s_waitcnt lgkmcnt(8)
	v_mfma_f32_32x32x16_bf16 v[38:53], v[144:147], v[78:81], v[38:53]
	s_waitcnt lgkmcnt(7)
	v_mfma_f32_32x32x16_bf16 v[54:69], v[54:57], v[82:85], 0
	s_waitcnt lgkmcnt(6)
	v_mfma_f32_32x32x16_bf16 v[54:69], v[148:151], v[78:81], v[54:69]
	s_waitcnt lgkmcnt(5)
	v_mfma_f32_32x32x16_bf16 v[38:53], v[152:155], v[74:77], v[38:53]
	s_waitcnt lgkmcnt(4)
	v_mfma_f32_32x32x16_bf16 v[54:69], v[156:159], v[74:77], v[54:69]
	s_waitcnt lgkmcnt(3)
	v_mfma_f32_32x32x16_bf16 v[38:53], v[160:163], v[70:73], v[38:53]
	s_waitcnt lgkmcnt(2)
	v_mfma_f32_32x32x16_bf16 v[54:69], v[164:167], v[70:73], v[54:69]
	s_waitcnt lgkmcnt(1)
	v_mfma_f32_32x32x16_bf16 v[38:53], v[168:171], v[86:89], v[38:53]
	s_waitcnt lgkmcnt(0)
	v_mfma_f32_32x32x16_bf16 v[54:69], v[172:175], v[86:89], v[54:69]
	s_nop 11
	v_max_i32_e32 v2, v38, v54
	v_max3_i32 v2, v2, v39, v55
	v_max3_i32 v2, v2, v40, v56
	v_max3_i32 v2, v2, v41, v57
	v_max3_i32 v2, v2, v42, v58
	v_max3_i32 v2, v2, v43, v59
	v_max3_i32 v2, v2, v44, v60
	v_max3_i32 v2, v2, v45, v61
	v_max3_i32 v2, v2, v46, v62
	v_max3_i32 v2, v2, v47, v63
	v_max3_i32 v2, v2, v48, v64
	v_max3_i32 v2, v2, v49, v65
	v_max3_i32 v2, v2, v50, v66
	v_max3_i32 v2, v2, v51, v67
	v_max3_i32 v2, v2, v52, v68
	v_max3_i32 v2, v2, v53, v69
	v_mov_b32_e32 v5, v2
	s_nop 1
	v_permlane32_swap_b32_e32 v2, v5
	v_max_i32_e32 v2, v2, v5
	v_cmp_lt_f32_e32 vcc, s29, v2
	s_cbranch_vccz .LBB0_771
	v_mov_b32_e32 v95, v4
	s_and_saveexec_b64 s[10:11], vcc
	s_cbranch_execz .LBB0_770
	v_add_f32_e32 v2, v4, v2
	v_cvt_pk_bf16_f32 v2, v2, 0
	v_lshlrev_b32_e32 v95, 16, v2
	s_branch .LBB0_770

.LBB0_778:
	ds_read_b128 v[178:181], v99 offset:9216
	ds_read_b128 v[182:185], v99 offset:9248
	ds_read_b128 v[186:189], v99 offset:13824
	ds_read_b128 v[190:193], v99 offset:13856
	ds_read_b128 v[194:197], v99 offset:9280
	ds_read_b128 v[198:201], v99 offset:13888
	ds_read_b128 v[202:205], v99 offset:9312
	ds_read_b128 v[206:209], v99 offset:13920
	v_exp_f32_e32 v38, v38
	v_exp_f32_e32 v39, v39
	v_exp_f32_e32 v54, v54
	v_exp_f32_e32 v55, v55
	v_exp_f32_e32 v40, v40
	v_exp_f32_e32 v41, v41
	v_exp_f32_e32 v56, v56
	v_exp_f32_e32 v57, v57
	v_exp_f32_e32 v42, v42
	v_exp_f32_e32 v43, v43
	v_exp_f32_e32 v102, v50
	v_exp_f32_e32 v103, v51
	v_pk_add_f32 v[50:51], v[132:133], v[38:39]
	v_exp_f32_e32 v58, v58
	v_exp_f32_e32 v59, v59
	v_pk_add_f32 v[50:51], v[54:55], v[50:51]
	v_exp_f32_e32 v44, v44
	v_exp_f32_e32 v45, v45
	v_pk_add_f32 v[50:51], v[40:41], v[50:51]
	v_exp_f32_e32 v60, v60
	v_exp_f32_e32 v61, v61
	v_pk_add_f32 v[50:51], v[56:57], v[50:51]
	v_exp_f32_e32 v46, v46
	v_exp_f32_e32 v47, v47
	v_pk_add_f32 v[50:51], v[42:43], v[50:51]
	v_exp_f32_e32 v62, v62
	v_exp_f32_e32 v63, v63
	v_pk_add_f32 v[50:51], v[58:59], v[50:51]
	v_exp_f32_e32 v48, v48
	v_exp_f32_e32 v49, v49
	v_pk_add_f32 v[50:51], v[44:45], v[50:51]
	v_exp_f32_e32 v64, v64
	v_exp_f32_e32 v65, v65
	v_pk_add_f32 v[50:51], v[60:61], v[50:51]
	v_exp_f32_e32 v66, v66
	v_pk_add_f32 v[50:51], v[46:47], v[50:51]
	v_exp_f32_e32 v67, v67
	v_pk_add_f32 v[50:51], v[62:63], v[50:51]
	v_exp_f32_e32 v104, v52
	v_exp_f32_e32 v105, v53
	v_pk_add_f32 v[50:51], v[48:49], v[50:51]
	v_exp_f32_e32 v68, v68
	v_exp_f32_e32 v69, v69
	v_pk_add_f32 v[50:51], v[64:65], v[50:51]
	v_cvt_pk_bf16_f32 v52, v42, v43
	v_pk_add_f32 v[50:51], v[102:103], v[50:51]
	v_cvt_pk_bf16_f32 v53, v44, v45
	v_cvt_pk_bf16_f32 v42, v54, v55
	v_cvt_pk_bf16_f32 v43, v56, v57
	v_cvt_pk_bf16_f32 v44, v58, v59
	v_cvt_pk_bf16_f32 v45, v60, v61
	v_pk_add_f32 v[50:51], v[66:67], v[50:51]
	v_cvt_pk_bf16_f32 v46, v46, v47
	v_pk_add_f32 v[50:51], v[104:105], v[50:51]
	v_cvt_pk_bf16_f32 v47, v48, v49
	v_pk_add_f32 v[132:133], v[68:69], v[50:51]
	v_cvt_pk_bf16_f32 v50, v38, v39
	v_cvt_pk_bf16_f32 v51, v40, v41
	v_cvt_pk_bf16_f32 v48, v102, v103
	v_cvt_pk_bf16_f32 v49, v104, v105
	s_waitcnt lgkmcnt(0)
	v_mfma_f32_32x32x16_bf16 v[6:21], v[178:181], v[50:53], v[6:21]
	v_cvt_pk_bf16_f32 v38, v62, v63
	v_cvt_pk_bf16_f32 v39, v64, v65
	v_cvt_pk_bf16_f32 v40, v66, v67
	v_cvt_pk_bf16_f32 v41, v68, v69
	v_mfma_f32_32x32x16_bf16 v[22:37], v[186:189], v[50:53], v[22:37]
	v_mfma_f32_32x32x16_bf16 v[6:21], v[182:185], v[46:49], v[6:21]
	v_mfma_f32_32x32x16_bf16 v[22:37], v[190:193], v[46:49], v[22:37]
	v_mfma_f32_32x32x16_bf16 v[6:21], v[194:197], v[42:45], v[6:21]
	v_mfma_f32_32x32x16_bf16 v[22:37], v[198:201], v[42:45], v[22:37]
	v_mfma_f32_32x32x16_bf16 v[6:21], v[202:205], v[38:41], v[6:21]
	v_mfma_f32_32x32x16_bf16 v[22:37], v[206:209], v[38:41], v[22:37]

.LBB0_780:
	s_add_i32 s10, s12, 63
	s_cmp_lt_i32 s10, s49
	s_cselect_b64 s[10:11], -1, 0
	s_cmp_gt_u32 s12, s52
	s_cselect_b64 s[38:39], -1, 0
	s_or_b64 s[10:11], s[10:11], s[38:39]
	s_and_b64 vcc, exec, s[10:11]
	s_cbranch_vccnz .LBB0_779
	ds_read_b128 v[38:41], v99
	ds_read_b128 v[102:105], v99 offset:32
	ds_read_b128 v[54:57], v99 offset:4608
	ds_read_b128 v[148:151], v99 offset:4640
	ds_read_b128 v[152:155], v99 offset:64
	ds_read_b128 v[156:159], v99 offset:4672
	ds_read_b128 v[160:163], v99 offset:96
	ds_read_b128 v[164:167], v99 offset:4704
	ds_read_b128 v[168:171], v99 offset:128
	ds_read_b128 v[172:175], v99 offset:4736
	s_cmp_lt_i32 s12, s53
	s_cselect_b64 s[10:11], -1, 0
	s_cmp_gt_u32 s12, s54
	s_cselect_b64 s[38:39], -1, 0
	s_or_b64 s[38:39], s[10:11], s[38:39]
	s_andn2_b64 vcc, exec, s[38:39]
	s_waitcnt lgkmcnt(9)
	v_mfma_f32_32x32x16_bf16 v[38:53], v[38:41], v[82:85], 0
	s_waitcnt lgkmcnt(8)
	v_mfma_f32_32x32x16_bf16 v[38:53], v[102:105], v[78:81], v[38:53]
	s_waitcnt lgkmcnt(7)
	v_mfma_f32_32x32x16_bf16 v[54:69], v[54:57], v[82:85], 0
	s_waitcnt lgkmcnt(6)
	v_mfma_f32_32x32x16_bf16 v[54:69], v[148:151], v[78:81], v[54:69]
	s_waitcnt lgkmcnt(5)
	v_mfma_f32_32x32x16_bf16 v[38:53], v[152:155], v[74:77], v[38:53]
	s_waitcnt lgkmcnt(4)
	v_mfma_f32_32x32x16_bf16 v[54:69], v[156:159], v[74:77], v[54:69]
	s_waitcnt lgkmcnt(3)
	v_mfma_f32_32x32x16_bf16 v[38:53], v[160:163], v[70:73], v[38:53]
	s_waitcnt lgkmcnt(2)
	v_mfma_f32_32x32x16_bf16 v[54:69], v[164:167], v[70:73], v[54:69]
	s_waitcnt lgkmcnt(1)
	v_mfma_f32_32x32x16_bf16 v[38:53], v[168:171], v[86:89], v[38:53]
	s_waitcnt lgkmcnt(0)
	v_mfma_f32_32x32x16_bf16 v[54:69], v[172:175], v[86:89], v[54:69]
	s_cbranch_vccnz .LBB0_783
	v_add_u32_e32 v2, s47, v100
	v_add_u32_e32 v5, -1, v2
	v_cmp_lt_u32_e32 vcc, s3, v5
	v_subrev_u32_e32 v5, 33, v2
	s_nop 3
	v_cndmask_b32_e32 v38, v224, v38, vcc
	v_cmp_lt_u32_e32 vcc, s3, v5
	v_add_u32_e32 v5, -2, v2
	s_nop 0
	v_cndmask_b32_e32 v54, v224, v54, vcc
	v_cmp_lt_u32_e32 vcc, s3, v5
	v_subrev_u32_e32 v5, 34, v2
	s_nop 0
	v_cndmask_b32_e32 v39, v224, v39, vcc
	v_cmp_lt_u32_e32 vcc, s3, v5
	v_add_u32_e32 v5, -3, v2
	s_nop 0
	v_cndmask_b32_e32 v55, v224, v55, vcc
	v_cmp_lt_u32_e32 vcc, s3, v5
	v_subrev_u32_e32 v5, 35, v2
	s_nop 0
	v_cndmask_b32_e32 v40, v224, v40, vcc
	v_cmp_lt_u32_e32 vcc, s3, v5
	v_add_u32_e32 v5, -4, v2
	s_nop 0
	v_cndmask_b32_e32 v56, v224, v56, vcc
	v_cmp_lt_u32_e32 vcc, s3, v5
	v_subrev_u32_e32 v5, 36, v2
	s_nop 0
	v_cndmask_b32_e32 v41, v224, v41, vcc
	v_cmp_lt_u32_e32 vcc, s3, v5
	v_add_u32_e32 v5, -9, v2
	s_nop 0
	v_cndmask_b32_e32 v57, v224, v57, vcc
	v_cmp_lt_u32_e32 vcc, s3, v5
	v_subrev_u32_e32 v5, 41, v2
	s_nop 0
	v_cndmask_b32_e32 v42, v224, v42, vcc
	v_cmp_lt_u32_e32 vcc, s3, v5
	v_add_u32_e32 v5, -10, v2
	s_nop 0
	v_cndmask_b32_e32 v58, v224, v58, vcc
	v_cmp_lt_u32_e32 vcc, s3, v5
	v_subrev_u32_e32 v5, 42, v2
	s_nop 0
	v_cndmask_b32_e32 v43, v224, v43, vcc
	v_cmp_lt_u32_e32 vcc, s3, v5
	v_add_u32_e32 v5, -11, v2
	s_nop 0
	v_cndmask_b32_e32 v59, v224, v59, vcc
	v_cmp_lt_u32_e32 vcc, s3, v5
	v_subrev_u32_e32 v5, 43, v2
	s_nop 0
	v_cndmask_b32_e32 v44, v224, v44, vcc
	v_cmp_lt_u32_e32 vcc, s3, v5
	v_add_u32_e32 v5, -12, v2
	s_nop 0
	v_cndmask_b32_e32 v60, v224, v60, vcc
	v_cmp_lt_u32_e32 vcc, s3, v5
	v_subrev_u32_e32 v5, 44, v2
	s_nop 0
	v_cndmask_b32_e32 v45, v224, v45, vcc
	v_cmp_lt_u32_e32 vcc, s3, v5
	v_subrev_u32_e32 v5, 17, v2
	s_nop 0
	v_cndmask_b32_e32 v61, v224, v61, vcc
	v_cmp_lt_u32_e32 vcc, s3, v5
	v_subrev_u32_e32 v5, 49, v2
	s_nop 0
	v_cndmask_b32_e32 v46, v224, v46, vcc
	v_cmp_lt_u32_e32 vcc, s3, v5
	v_subrev_u32_e32 v5, 18, v2
	s_nop 0
	v_cndmask_b32_e32 v62, v224, v62, vcc
	v_cmp_lt_u32_e32 vcc, s3, v5
	v_subrev_u32_e32 v5, 50, v2
	s_nop 0
	v_cndmask_b32_e32 v47, v224, v47, vcc
	v_cmp_lt_u32_e32 vcc, s3, v5
	v_subrev_u32_e32 v5, 19, v2
	s_nop 0
	v_cndmask_b32_e32 v63, v224, v63, vcc
	v_cmp_lt_u32_e32 vcc, s3, v5
	v_subrev_u32_e32 v5, 51, v2
	s_nop 0
	v_cndmask_b32_e32 v48, v224, v48, vcc
	v_cmp_lt_u32_e32 vcc, s3, v5
	v_subrev_u32_e32 v5, 20, v2
	s_nop 0
	v_cndmask_b32_e32 v64, v224, v64, vcc
	v_cmp_lt_u32_e32 vcc, s3, v5
	v_subrev_u32_e32 v5, 52, v2
	s_nop 0
	v_cndmask_b32_e32 v49, v224, v49, vcc
	v_cmp_lt_u32_e32 vcc, s3, v5
	v_subrev_u32_e32 v5, 25, v2
	s_nop 0
	v_cndmask_b32_e32 v65, v224, v65, vcc
	v_cmp_lt_u32_e32 vcc, s3, v5
	v_subrev_u32_e32 v5, 57, v2
	s_nop 0
	v_cndmask_b32_e32 v50, v224, v50, vcc
	v_cmp_lt_u32_e32 vcc, s3, v5
	v_subrev_u32_e32 v5, 26, v2
	s_nop 0
	v_cndmask_b32_e32 v66, v224, v66, vcc
	v_cmp_lt_u32_e32 vcc, s3, v5
	v_subrev_u32_e32 v5, 58, v2
	s_nop 0
	v_cndmask_b32_e32 v51, v224, v51, vcc
	v_cmp_lt_u32_e32 vcc, s3, v5
	v_subrev_u32_e32 v5, 27, v2
	s_nop 0
	v_cndmask_b32_e32 v67, v224, v67, vcc
	v_cmp_lt_u32_e32 vcc, s3, v5
	v_subrev_u32_e32 v5, 59, v2
	s_nop 0
	v_cndmask_b32_e32 v52, v224, v52, vcc
	v_cmp_lt_u32_e32 vcc, s3, v5
	v_subrev_u32_e32 v5, 28, v2
	v_subrev_u32_e32 v2, 60, v2
	v_cndmask_b32_e32 v68, v224, v68, vcc
	v_cmp_lt_u32_e32 vcc, s3, v5
	s_nop 1
	v_cndmask_b32_e32 v53, v224, v53, vcc
	v_cmp_lt_u32_e32 vcc, s3, v2
	s_nop 1
	v_cndmask_b32_e32 v69, v224, v69, vcc

.LBB0_796:
	ds_read_b128 v[178:181], v1 offset:9216
	ds_read_b128 v[182:185], v1 offset:9248
	ds_read_b128 v[186:189], v1 offset:13824
	ds_read_b128 v[190:193], v1 offset:13856
	ds_read_b128 v[194:197], v1 offset:9280
	ds_read_b128 v[198:201], v1 offset:13888
	ds_read_b128 v[202:205], v1 offset:9312
	ds_read_b128 v[206:209], v1 offset:13920
	v_exp_f32_e32 v4, v38
	v_exp_f32_e32 v5, v39
	v_exp_f32_e32 v38, v54
	v_exp_f32_e32 v39, v55
	v_exp_f32_e32 v40, v40
	v_exp_f32_e32 v41, v41
	v_exp_f32_e32 v54, v56
	v_exp_f32_e32 v55, v57
	v_exp_f32_e32 v42, v42
	v_exp_f32_e32 v56, v58
	v_exp_f32_e32 v43, v43
	v_exp_f32_e32 v57, v59
	v_exp_f32_e32 v58, v60
	v_exp_f32_e32 v59, v61
	v_exp_f32_e32 v60, v62
	v_exp_f32_e32 v61, v63
	v_exp_f32_e32 v62, v64
	v_exp_f32_e32 v63, v65
	v_exp_f32_e32 v64, v50
	v_exp_f32_e32 v65, v51
	v_pk_add_f32 v[50:51], v[132:133], v[4:5]
	v_exp_f32_e32 v44, v44
	v_pk_add_f32 v[50:51], v[38:39], v[50:51]
	v_exp_f32_e32 v45, v45
	v_pk_add_f32 v[50:51], v[40:41], v[50:51]
	v_exp_f32_e32 v46, v46
	v_pk_add_f32 v[50:51], v[54:55], v[50:51]
	v_exp_f32_e32 v47, v47
	v_pk_add_f32 v[50:51], v[42:43], v[50:51]
	v_exp_f32_e32 v48, v48
	v_pk_add_f32 v[50:51], v[56:57], v[50:51]
	v_exp_f32_e32 v49, v49
	v_pk_add_f32 v[50:51], v[44:45], v[50:51]
	v_exp_f32_e32 v66, v66
	v_pk_add_f32 v[50:51], v[58:59], v[50:51]
	v_exp_f32_e32 v67, v67
	v_pk_add_f32 v[50:51], v[46:47], v[50:51]
	v_exp_f32_e32 v70, v52
	v_pk_add_f32 v[50:51], v[60:61], v[50:51]
	v_exp_f32_e32 v71, v53
	v_pk_add_f32 v[50:51], v[48:49], v[50:51]
	v_exp_f32_e32 v68, v68
	v_exp_f32_e32 v69, v69
	v_pk_add_f32 v[50:51], v[62:63], v[50:51]
	v_cvt_pk_bf16_f32 v52, v42, v43
	v_pk_add_f32 v[50:51], v[64:65], v[50:51]
	v_cvt_pk_bf16_f32 v53, v44, v45
	v_cvt_pk_bf16_f32 v42, v38, v39
	v_cvt_pk_bf16_f32 v43, v54, v55
	v_cvt_pk_bf16_f32 v44, v56, v57
	v_cvt_pk_bf16_f32 v45, v58, v59
	v_cvt_pk_bf16_f32 v38, v60, v61
	v_pk_add_f32 v[50:51], v[66:67], v[50:51]
	v_cvt_pk_bf16_f32 v46, v46, v47
	v_pk_add_f32 v[50:51], v[70:71], v[50:51]
	v_cvt_pk_bf16_f32 v47, v48, v49
	v_pk_add_f32 v[132:133], v[68:69], v[50:51]
	v_cvt_pk_bf16_f32 v50, v4, v5
	v_cvt_pk_bf16_f32 v51, v40, v41
	v_cvt_pk_bf16_f32 v48, v64, v65
	v_cvt_pk_bf16_f32 v49, v70, v71
	s_waitcnt lgkmcnt(0)
	v_mfma_f32_32x32x16_bf16 v[6:21], v[178:181], v[50:53], v[6:21]
	v_cvt_pk_bf16_f32 v39, v62, v63
	v_cvt_pk_bf16_f32 v40, v66, v67
	v_cvt_pk_bf16_f32 v41, v68, v69
	v_mfma_f32_32x32x16_bf16 v[22:37], v[186:189], v[50:53], v[22:37]
	v_mfma_f32_32x32x16_bf16 v[6:21], v[182:185], v[46:49], v[6:21]
	v_mfma_f32_32x32x16_bf16 v[22:37], v[190:193], v[46:49], v[22:37]
	v_mfma_f32_32x32x16_bf16 v[6:21], v[194:197], v[42:45], v[6:21]
	v_mfma_f32_32x32x16_bf16 v[22:37], v[198:201], v[42:45], v[22:37]
	v_mfma_f32_32x32x16_bf16 v[6:21], v[202:205], v[38:41], v[6:21]
	v_mfma_f32_32x32x16_bf16 v[22:37], v[206:209], v[38:41], v[22:37]
	s_branch .LBB0_768

.LBB0_798:
	ds_read_b128 v[178:181], v1 offset:9216
	ds_read_b128 v[182:185], v1 offset:9248
	ds_read_b128 v[186:189], v1 offset:13824
	ds_read_b128 v[190:193], v1 offset:13856
	ds_read_b128 v[194:197], v1 offset:9280
	ds_read_b128 v[198:201], v1 offset:13888
	ds_read_b128 v[202:205], v1 offset:9312
	ds_read_b128 v[206:209], v1 offset:13920
	v_exp_f32_e32 v4, v38
	v_exp_f32_e32 v5, v39
	v_exp_f32_e32 v38, v54
	v_exp_f32_e32 v39, v55
	v_exp_f32_e32 v40, v40
	v_exp_f32_e32 v41, v41
	v_exp_f32_e32 v54, v56
	v_exp_f32_e32 v55, v57
	v_exp_f32_e32 v42, v42
	v_exp_f32_e32 v56, v58
	v_exp_f32_e32 v43, v43
	v_exp_f32_e32 v57, v59
	v_exp_f32_e32 v58, v60
	v_exp_f32_e32 v59, v61
	v_exp_f32_e32 v60, v62
	v_exp_f32_e32 v61, v63
	v_exp_f32_e32 v62, v64
	v_exp_f32_e32 v63, v65
	v_exp_f32_e32 v64, v50
	v_exp_f32_e32 v65, v51
	v_pk_add_f32 v[50:51], v[126:127], v[4:5]
	v_exp_f32_e32 v44, v44
	v_pk_add_f32 v[50:51], v[38:39], v[50:51]
	v_exp_f32_e32 v45, v45
	v_pk_add_f32 v[50:51], v[40:41], v[50:51]
	v_exp_f32_e32 v46, v46
	v_pk_add_f32 v[50:51], v[54:55], v[50:51]
	v_exp_f32_e32 v47, v47
	v_pk_add_f32 v[50:51], v[42:43], v[50:51]
	v_exp_f32_e32 v48, v48
	v_pk_add_f32 v[50:51], v[56:57], v[50:51]
	v_exp_f32_e32 v49, v49
	v_pk_add_f32 v[50:51], v[44:45], v[50:51]
	v_exp_f32_e32 v66, v66
	v_pk_add_f32 v[50:51], v[58:59], v[50:51]
	v_exp_f32_e32 v67, v67
	v_pk_add_f32 v[50:51], v[46:47], v[50:51]
	v_exp_f32_e32 v70, v52
	v_pk_add_f32 v[50:51], v[60:61], v[50:51]
	v_exp_f32_e32 v71, v53
	v_pk_add_f32 v[50:51], v[48:49], v[50:51]
	v_exp_f32_e32 v68, v68
	v_exp_f32_e32 v69, v69
	v_pk_add_f32 v[50:51], v[62:63], v[50:51]
	v_cvt_pk_bf16_f32 v52, v42, v43
	v_pk_add_f32 v[50:51], v[64:65], v[50:51]
	v_cvt_pk_bf16_f32 v53, v44, v45
	v_cvt_pk_bf16_f32 v42, v38, v39
	v_cvt_pk_bf16_f32 v43, v54, v55
	v_cvt_pk_bf16_f32 v44, v56, v57
	v_cvt_pk_bf16_f32 v45, v58, v59
	v_cvt_pk_bf16_f32 v38, v60, v61
	v_pk_add_f32 v[50:51], v[66:67], v[50:51]
	v_cvt_pk_bf16_f32 v46, v46, v47
	v_pk_add_f32 v[50:51], v[70:71], v[50:51]
	v_cvt_pk_bf16_f32 v47, v48, v49
	v_pk_add_f32 v[126:127], v[68:69], v[50:51]
	v_cvt_pk_bf16_f32 v50, v4, v5
	v_cvt_pk_bf16_f32 v51, v40, v41
	v_cvt_pk_bf16_f32 v48, v64, v65
	v_cvt_pk_bf16_f32 v49, v70, v71
	s_waitcnt lgkmcnt(0)
	v_mfma_f32_32x32x16_bf16 v[6:21], v[178:181], v[50:53], v[6:21]
	v_cvt_pk_bf16_f32 v39, v62, v63
	v_cvt_pk_bf16_f32 v40, v66, v67
	v_cvt_pk_bf16_f32 v41, v68, v69
	v_mfma_f32_32x32x16_bf16 v[22:37], v[186:189], v[50:53], v[22:37]
	v_mfma_f32_32x32x16_bf16 v[6:21], v[182:185], v[46:49], v[6:21]
	v_mfma_f32_32x32x16_bf16 v[22:37], v[190:193], v[46:49], v[22:37]
	v_mfma_f32_32x32x16_bf16 v[6:21], v[194:197], v[42:45], v[6:21]
	v_mfma_f32_32x32x16_bf16 v[22:37], v[198:201], v[42:45], v[22:37]
	v_mfma_f32_32x32x16_bf16 v[6:21], v[202:205], v[38:41], v[6:21]
	v_mfma_f32_32x32x16_bf16 v[22:37], v[206:209], v[38:41], v[22:37]

.LBB0_804:
	ds_read_b128 v[178:181], v131 offset:9216
	ds_read_b128 v[182:185], v131 offset:9248
	ds_read_b128 v[186:189], v131 offset:13824
	ds_read_b128 v[190:193], v131 offset:13856
	ds_read_b128 v[194:197], v131 offset:9280
	ds_read_b128 v[198:201], v131 offset:13888
	ds_read_b128 v[202:205], v131 offset:9312
	ds_read_b128 v[206:209], v131 offset:13920
	v_exp_f32_e32 v38, v38
	v_exp_f32_e32 v39, v39
	v_exp_f32_e32 v54, v54
	v_exp_f32_e32 v55, v55
	v_exp_f32_e32 v40, v40
	v_exp_f32_e32 v41, v41
	v_exp_f32_e32 v56, v56
	v_exp_f32_e32 v57, v57
	v_exp_f32_e32 v42, v42
	v_exp_f32_e32 v43, v43
	v_exp_f32_e32 v142, v50
	v_exp_f32_e32 v143, v51
	v_pk_add_f32 v[50:51], v[126:127], v[38:39]
	v_exp_f32_e32 v58, v58
	v_exp_f32_e32 v59, v59
	v_pk_add_f32 v[50:51], v[54:55], v[50:51]
	v_exp_f32_e32 v44, v44
	v_exp_f32_e32 v45, v45
	v_pk_add_f32 v[50:51], v[40:41], v[50:51]
	v_exp_f32_e32 v60, v60
	v_exp_f32_e32 v61, v61
	v_pk_add_f32 v[50:51], v[56:57], v[50:51]
	v_exp_f32_e32 v46, v46
	v_exp_f32_e32 v47, v47
	v_pk_add_f32 v[50:51], v[42:43], v[50:51]
	v_exp_f32_e32 v62, v62
	v_exp_f32_e32 v63, v63
	v_pk_add_f32 v[50:51], v[58:59], v[50:51]
	v_exp_f32_e32 v48, v48
	v_exp_f32_e32 v49, v49
	v_pk_add_f32 v[50:51], v[44:45], v[50:51]
	v_exp_f32_e32 v64, v64
	v_exp_f32_e32 v65, v65
	v_pk_add_f32 v[50:51], v[60:61], v[50:51]
	v_exp_f32_e32 v66, v66
	v_pk_add_f32 v[50:51], v[46:47], v[50:51]
	v_exp_f32_e32 v67, v67
	v_pk_add_f32 v[50:51], v[62:63], v[50:51]
	v_exp_f32_e32 v144, v52
	v_exp_f32_e32 v145, v53
	v_pk_add_f32 v[50:51], v[48:49], v[50:51]
	v_exp_f32_e32 v68, v68
	v_exp_f32_e32 v69, v69
	v_pk_add_f32 v[50:51], v[64:65], v[50:51]
	v_cvt_pk_bf16_f32 v52, v42, v43
	v_pk_add_f32 v[50:51], v[142:143], v[50:51]
	v_cvt_pk_bf16_f32 v53, v44, v45
	v_cvt_pk_bf16_f32 v42, v54, v55
	v_cvt_pk_bf16_f32 v43, v56, v57
	v_cvt_pk_bf16_f32 v44, v58, v59
	v_cvt_pk_bf16_f32 v45, v60, v61
	v_pk_add_f32 v[50:51], v[66:67], v[50:51]
	v_cvt_pk_bf16_f32 v46, v46, v47
	v_pk_add_f32 v[50:51], v[144:145], v[50:51]
	v_cvt_pk_bf16_f32 v47, v48, v49
	v_pk_add_f32 v[126:127], v[68:69], v[50:51]
	v_cvt_pk_bf16_f32 v50, v38, v39
	v_cvt_pk_bf16_f32 v51, v40, v41
	v_cvt_pk_bf16_f32 v48, v142, v143
	v_cvt_pk_bf16_f32 v49, v144, v145
	s_waitcnt lgkmcnt(0)
	v_mfma_f32_32x32x16_bf16 v[6:21], v[178:181], v[50:53], v[6:21]
	v_cvt_pk_bf16_f32 v38, v62, v63
	v_cvt_pk_bf16_f32 v39, v64, v65
	v_cvt_pk_bf16_f32 v40, v66, v67
	v_cvt_pk_bf16_f32 v41, v68, v69
	s_addk_i32 s12, 0x4800
	s_cmp_eq_u32 s12, 0x12000
	v_mfma_f32_32x32x16_bf16 v[22:37], v[186:189], v[50:53], v[22:37]
	v_mfma_f32_32x32x16_bf16 v[6:21], v[182:185], v[46:49], v[6:21]
	v_mfma_f32_32x32x16_bf16 v[22:37], v[190:193], v[46:49], v[22:37]
	v_mfma_f32_32x32x16_bf16 v[6:21], v[194:197], v[42:45], v[6:21]
	v_mfma_f32_32x32x16_bf16 v[22:37], v[198:201], v[42:45], v[22:37]
	v_mfma_f32_32x32x16_bf16 v[6:21], v[202:205], v[38:41], v[6:21]
	v_mfma_f32_32x32x16_bf16 v[22:37], v[206:209], v[38:41], v[22:37]
	s_cbranch_scc1 .LBB0_808
.LBB0_805:
	v_add_u32_e32 v131, s12, v1
	ds_read_b128 v[38:41], v131
	ds_read_b128 v[142:145], v131 offset:32
	ds_read_b128 v[54:57], v131 offset:4608
	ds_read_b128 v[148:151], v131 offset:4640
	ds_read_b128 v[152:155], v131 offset:64
	ds_read_b128 v[156:159], v131 offset:4672
	ds_read_b128 v[160:163], v131 offset:96
	ds_read_b128 v[164:167], v131 offset:4704
	ds_read_b128 v[168:171], v131 offset:128
	ds_read_b128 v[172:175], v131 offset:4736
	s_waitcnt lgkmcnt(9)
	v_mfma_f32_32x32x16_bf16 v[38:53], v[38:41], v[82:85], 0
	s_waitcnt lgkmcnt(8)
	v_mfma_f32_32x32x16_bf16 v[38:53], v[142:145], v[78:81], v[38:53]
	s_waitcnt lgkmcnt(7)
	v_mfma_f32_32x32x16_bf16 v[54:69], v[54:57], v[82:85], 0
	s_waitcnt lgkmcnt(6)
	v_mfma_f32_32x32x16_bf16 v[54:69], v[148:151], v[78:81], v[54:69]
	s_waitcnt lgkmcnt(5)
	v_mfma_f32_32x32x16_bf16 v[38:53], v[152:155], v[74:77], v[38:53]
	s_waitcnt lgkmcnt(4)
	v_mfma_f32_32x32x16_bf16 v[54:69], v[156:159], v[74:77], v[54:69]
	s_waitcnt lgkmcnt(3)
	v_mfma_f32_32x32x16_bf16 v[38:53], v[160:163], v[70:73], v[38:53]
	s_waitcnt lgkmcnt(2)
	v_mfma_f32_32x32x16_bf16 v[54:69], v[164:167], v[70:73], v[54:69]
	s_waitcnt lgkmcnt(1)
	v_mfma_f32_32x32x16_bf16 v[38:53], v[168:171], v[86:89], v[38:53]
	s_waitcnt lgkmcnt(0)
	v_mfma_f32_32x32x16_bf16 v[54:69], v[172:175], v[86:89], v[54:69]
	s_nop 11
	v_max_i32_e32 v2, v38, v54
	v_max3_i32 v2, v2, v39, v55
	v_max3_i32 v2, v2, v40, v56
	v_max3_i32 v2, v2, v41, v57
	v_max3_i32 v2, v2, v42, v58
	v_max3_i32 v2, v2, v43, v59
	v_max3_i32 v2, v2, v44, v60
	v_max3_i32 v2, v2, v45, v61
	v_max3_i32 v2, v2, v46, v62
	v_max3_i32 v2, v2, v47, v63
	v_max3_i32 v2, v2, v48, v64
	v_max3_i32 v2, v2, v49, v65
	v_max3_i32 v2, v2, v50, v66
	v_max3_i32 v2, v2, v51, v67
	v_max3_i32 v2, v2, v52, v68
	v_max3_i32 v2, v2, v53, v69
	v_mov_b32_e32 v5, v2
	s_nop 1
	v_permlane32_swap_b32_e32 v2, v5
	v_max_i32_e32 v2, v2, v5
	v_cmp_lt_f32_e32 vcc, s29, v2
	s_cbranch_vccz .LBB0_804
	v_mov_b32_e32 v141, v4
	s_and_saveexec_b64 s[10:11], vcc
	s_cbranch_execz .LBB0_803
	v_add_f32_e32 v2, v4, v2
	v_cvt_pk_bf16_f32 v2, v2, 0
	v_lshlrev_b32_e32 v141, 16, v2
	s_branch .LBB0_803

.LBB0_812:
	ds_read_b128 v[178:181], v98 offset:9216
	ds_read_b128 v[182:185], v98 offset:9248
	ds_read_b128 v[186:189], v98 offset:13824
	ds_read_b128 v[190:193], v98 offset:13856
	ds_read_b128 v[194:197], v98 offset:9280
	ds_read_b128 v[198:201], v98 offset:13888
	ds_read_b128 v[202:205], v98 offset:9312
	ds_read_b128 v[206:209], v98 offset:13920
	v_exp_f32_e32 v38, v38
	v_exp_f32_e32 v39, v39
	v_exp_f32_e32 v54, v54
	v_exp_f32_e32 v55, v55
	v_exp_f32_e32 v40, v40
	v_exp_f32_e32 v41, v41
	v_exp_f32_e32 v56, v56
	v_exp_f32_e32 v57, v57
	v_exp_f32_e32 v42, v42
	v_exp_f32_e32 v43, v43
	v_exp_f32_e32 v100, v50
	v_exp_f32_e32 v101, v51
	v_pk_add_f32 v[50:51], v[126:127], v[38:39]
	v_exp_f32_e32 v58, v58
	v_exp_f32_e32 v59, v59
	v_pk_add_f32 v[50:51], v[54:55], v[50:51]
	v_exp_f32_e32 v44, v44
	v_exp_f32_e32 v45, v45
	v_pk_add_f32 v[50:51], v[40:41], v[50:51]
	v_exp_f32_e32 v60, v60
	v_exp_f32_e32 v61, v61
	v_pk_add_f32 v[50:51], v[56:57], v[50:51]
	v_exp_f32_e32 v46, v46
	v_exp_f32_e32 v47, v47
	v_pk_add_f32 v[50:51], v[42:43], v[50:51]
	v_exp_f32_e32 v62, v62
	v_exp_f32_e32 v63, v63
	v_pk_add_f32 v[50:51], v[58:59], v[50:51]
	v_exp_f32_e32 v48, v48
	v_exp_f32_e32 v49, v49
	v_pk_add_f32 v[50:51], v[44:45], v[50:51]
	v_exp_f32_e32 v64, v64
	v_exp_f32_e32 v65, v65
	v_pk_add_f32 v[50:51], v[60:61], v[50:51]
	v_exp_f32_e32 v66, v66
	v_pk_add_f32 v[50:51], v[46:47], v[50:51]
	v_exp_f32_e32 v67, v67
	v_pk_add_f32 v[50:51], v[62:63], v[50:51]
	v_exp_f32_e32 v102, v52
	v_exp_f32_e32 v103, v53
	v_pk_add_f32 v[50:51], v[48:49], v[50:51]
	v_exp_f32_e32 v68, v68
	v_exp_f32_e32 v69, v69
	v_pk_add_f32 v[50:51], v[64:65], v[50:51]
	v_cvt_pk_bf16_f32 v52, v42, v43
	v_pk_add_f32 v[50:51], v[100:101], v[50:51]
	v_cvt_pk_bf16_f32 v53, v44, v45
	v_cvt_pk_bf16_f32 v42, v54, v55
	v_cvt_pk_bf16_f32 v43, v56, v57
	v_cvt_pk_bf16_f32 v44, v58, v59
	v_cvt_pk_bf16_f32 v45, v60, v61
	v_pk_add_f32 v[50:51], v[66:67], v[50:51]
	v_cvt_pk_bf16_f32 v46, v46, v47
	v_pk_add_f32 v[50:51], v[102:103], v[50:51]
	v_cvt_pk_bf16_f32 v47, v48, v49
	v_pk_add_f32 v[126:127], v[68:69], v[50:51]
	v_cvt_pk_bf16_f32 v50, v38, v39
	v_cvt_pk_bf16_f32 v51, v40, v41
	v_cvt_pk_bf16_f32 v48, v100, v101
	v_cvt_pk_bf16_f32 v49, v102, v103
	s_waitcnt lgkmcnt(0)
	v_mfma_f32_32x32x16_bf16 v[6:21], v[178:181], v[50:53], v[6:21]
	v_cvt_pk_bf16_f32 v38, v62, v63
	v_cvt_pk_bf16_f32 v39, v64, v65
	v_cvt_pk_bf16_f32 v40, v66, v67
	v_cvt_pk_bf16_f32 v41, v68, v69
	v_mfma_f32_32x32x16_bf16 v[22:37], v[186:189], v[50:53], v[22:37]
	v_mfma_f32_32x32x16_bf16 v[6:21], v[182:185], v[46:49], v[6:21]
	v_mfma_f32_32x32x16_bf16 v[22:37], v[190:193], v[46:49], v[22:37]
	v_mfma_f32_32x32x16_bf16 v[6:21], v[194:197], v[42:45], v[6:21]
	v_mfma_f32_32x32x16_bf16 v[22:37], v[198:201], v[42:45], v[22:37]
	v_mfma_f32_32x32x16_bf16 v[6:21], v[202:205], v[38:41], v[6:21]
	v_mfma_f32_32x32x16_bf16 v[22:37], v[206:209], v[38:41], v[22:37]

.LBB0_814:
	s_add_i32 s10, s55, 63
	s_cmp_lt_i32 s10, s12
	s_cselect_b64 s[10:11], -1, 0
	s_cmp_gt_u32 s55, s40
	s_cselect_b64 s[38:39], -1, 0
	s_or_b64 s[10:11], s[10:11], s[38:39]
	s_and_b64 vcc, exec, s[10:11]
	s_cbranch_vccnz .LBB0_813
	ds_read_b128 v[38:41], v98
	ds_read_b128 v[100:103], v98 offset:32
	ds_read_b128 v[54:57], v98 offset:4608
	ds_read_b128 v[148:151], v98 offset:4640
	ds_read_b128 v[152:155], v98 offset:64
	ds_read_b128 v[156:159], v98 offset:4672
	ds_read_b128 v[160:163], v98 offset:96
	ds_read_b128 v[164:167], v98 offset:4704
	ds_read_b128 v[168:171], v98 offset:128
	ds_read_b128 v[172:175], v98 offset:4736
	s_cmp_lt_i32 s55, s41
	s_cselect_b64 s[10:11], -1, 0
	s_cmp_gt_u32 s55, s44
	s_cselect_b64 s[38:39], -1, 0
	s_or_b64 s[38:39], s[10:11], s[38:39]
	s_andn2_b64 vcc, exec, s[38:39]
	s_waitcnt lgkmcnt(9)
	v_mfma_f32_32x32x16_bf16 v[38:53], v[38:41], v[82:85], 0
	s_waitcnt lgkmcnt(8)
	v_mfma_f32_32x32x16_bf16 v[38:53], v[100:103], v[78:81], v[38:53]
	s_waitcnt lgkmcnt(7)
	v_mfma_f32_32x32x16_bf16 v[54:69], v[54:57], v[82:85], 0
	s_waitcnt lgkmcnt(6)
	v_mfma_f32_32x32x16_bf16 v[54:69], v[148:151], v[78:81], v[54:69]
	s_waitcnt lgkmcnt(5)
	v_mfma_f32_32x32x16_bf16 v[38:53], v[152:155], v[74:77], v[38:53]
	s_waitcnt lgkmcnt(4)
	v_mfma_f32_32x32x16_bf16 v[54:69], v[156:159], v[74:77], v[54:69]
	s_waitcnt lgkmcnt(3)
	v_mfma_f32_32x32x16_bf16 v[38:53], v[160:163], v[70:73], v[38:53]
	s_waitcnt lgkmcnt(2)
	v_mfma_f32_32x32x16_bf16 v[54:69], v[164:167], v[70:73], v[54:69]
	s_waitcnt lgkmcnt(1)
	v_mfma_f32_32x32x16_bf16 v[38:53], v[168:171], v[86:89], v[38:53]
	s_waitcnt lgkmcnt(0)
	v_mfma_f32_32x32x16_bf16 v[54:69], v[172:175], v[86:89], v[54:69]
	s_cbranch_vccnz .LBB0_817
	v_add_u32_e32 v2, s46, v99
	v_add_u32_e32 v5, -1, v2
	v_cmp_lt_u32_e32 vcc, s3, v5
	v_subrev_u32_e32 v5, 33, v2
	s_nop 3
	v_cndmask_b32_e32 v38, v224, v38, vcc
	v_cmp_lt_u32_e32 vcc, s3, v5
	v_add_u32_e32 v5, -2, v2
	s_nop 0
	v_cndmask_b32_e32 v54, v224, v54, vcc
	v_cmp_lt_u32_e32 vcc, s3, v5
	v_subrev_u32_e32 v5, 34, v2
	s_nop 0
	v_cndmask_b32_e32 v39, v224, v39, vcc
	v_cmp_lt_u32_e32 vcc, s3, v5
	v_add_u32_e32 v5, -3, v2
	s_nop 0
	v_cndmask_b32_e32 v55, v224, v55, vcc
	v_cmp_lt_u32_e32 vcc, s3, v5
	v_subrev_u32_e32 v5, 35, v2
	s_nop 0
	v_cndmask_b32_e32 v40, v224, v40, vcc
	v_cmp_lt_u32_e32 vcc, s3, v5
	v_add_u32_e32 v5, -4, v2
	s_nop 0
	v_cndmask_b32_e32 v56, v224, v56, vcc
	v_cmp_lt_u32_e32 vcc, s3, v5
	v_subrev_u32_e32 v5, 36, v2
	s_nop 0
	v_cndmask_b32_e32 v41, v224, v41, vcc
	v_cmp_lt_u32_e32 vcc, s3, v5
	v_add_u32_e32 v5, -9, v2
	s_nop 0
	v_cndmask_b32_e32 v57, v224, v57, vcc
	v_cmp_lt_u32_e32 vcc, s3, v5
	v_subrev_u32_e32 v5, 41, v2
	s_nop 0
	v_cndmask_b32_e32 v42, v224, v42, vcc
	v_cmp_lt_u32_e32 vcc, s3, v5
	v_add_u32_e32 v5, -10, v2
	s_nop 0
	v_cndmask_b32_e32 v58, v224, v58, vcc
	v_cmp_lt_u32_e32 vcc, s3, v5
	v_subrev_u32_e32 v5, 42, v2
	s_nop 0
	v_cndmask_b32_e32 v43, v224, v43, vcc
	v_cmp_lt_u32_e32 vcc, s3, v5
	v_add_u32_e32 v5, -11, v2
	s_nop 0
	v_cndmask_b32_e32 v59, v224, v59, vcc
	v_cmp_lt_u32_e32 vcc, s3, v5
	v_subrev_u32_e32 v5, 43, v2
	s_nop 0
	v_cndmask_b32_e32 v44, v224, v44, vcc
	v_cmp_lt_u32_e32 vcc, s3, v5
	v_add_u32_e32 v5, -12, v2
	s_nop 0
	v_cndmask_b32_e32 v60, v224, v60, vcc
	v_cmp_lt_u32_e32 vcc, s3, v5
	v_subrev_u32_e32 v5, 44, v2
	s_nop 0
	v_cndmask_b32_e32 v45, v224, v45, vcc
	v_cmp_lt_u32_e32 vcc, s3, v5
	v_subrev_u32_e32 v5, 17, v2
	s_nop 0
	v_cndmask_b32_e32 v61, v224, v61, vcc
	v_cmp_lt_u32_e32 vcc, s3, v5
	v_subrev_u32_e32 v5, 49, v2
	s_nop 0
	v_cndmask_b32_e32 v46, v224, v46, vcc
	v_cmp_lt_u32_e32 vcc, s3, v5
	v_subrev_u32_e32 v5, 18, v2
	s_nop 0
	v_cndmask_b32_e32 v62, v224, v62, vcc
	v_cmp_lt_u32_e32 vcc, s3, v5
	v_subrev_u32_e32 v5, 50, v2
	s_nop 0
	v_cndmask_b32_e32 v47, v224, v47, vcc
	v_cmp_lt_u32_e32 vcc, s3, v5
	v_subrev_u32_e32 v5, 19, v2
	s_nop 0
	v_cndmask_b32_e32 v63, v224, v63, vcc
	v_cmp_lt_u32_e32 vcc, s3, v5
	v_subrev_u32_e32 v5, 51, v2
	s_nop 0
	v_cndmask_b32_e32 v48, v224, v48, vcc
	v_cmp_lt_u32_e32 vcc, s3, v5
	v_subrev_u32_e32 v5, 20, v2
	s_nop 0
	v_cndmask_b32_e32 v64, v224, v64, vcc
	v_cmp_lt_u32_e32 vcc, s3, v5
	v_subrev_u32_e32 v5, 52, v2
	s_nop 0
	v_cndmask_b32_e32 v49, v224, v49, vcc
	v_cmp_lt_u32_e32 vcc, s3, v5
	v_subrev_u32_e32 v5, 25, v2
	s_nop 0
	v_cndmask_b32_e32 v65, v224, v65, vcc
	v_cmp_lt_u32_e32 vcc, s3, v5
	v_subrev_u32_e32 v5, 57, v2
	s_nop 0
	v_cndmask_b32_e32 v50, v224, v50, vcc
	v_cmp_lt_u32_e32 vcc, s3, v5
	v_subrev_u32_e32 v5, 26, v2
	s_nop 0
	v_cndmask_b32_e32 v66, v224, v66, vcc
	v_cmp_lt_u32_e32 vcc, s3, v5
	v_subrev_u32_e32 v5, 58, v2
	s_nop 0
	v_cndmask_b32_e32 v51, v224, v51, vcc
	v_cmp_lt_u32_e32 vcc, s3, v5
	v_subrev_u32_e32 v5, 27, v2
	s_nop 0
	v_cndmask_b32_e32 v67, v224, v67, vcc
	v_cmp_lt_u32_e32 vcc, s3, v5
	v_subrev_u32_e32 v5, 59, v2
	s_nop 0
	v_cndmask_b32_e32 v52, v224, v52, vcc
	v_cmp_lt_u32_e32 vcc, s3, v5
	v_subrev_u32_e32 v5, 28, v2
	v_subrev_u32_e32 v2, 60, v2
	v_cndmask_b32_e32 v68, v224, v68, vcc
	v_cmp_lt_u32_e32 vcc, s3, v5
	s_nop 1
	v_cndmask_b32_e32 v53, v224, v53, vcc
	v_cmp_lt_u32_e32 vcc, s3, v2
	s_nop 1
	v_cndmask_b32_e32 v69, v224, v69, vcc

.LBB0_833:
	s_add_i32 s10, s46, 63
	s_cmp_lt_i32 s10, s40
	s_cselect_b64 s[10:11], -1, 0
	s_cmp_gt_u32 s46, s41
	s_cselect_b64 s[38:39], -1, 0
	s_or_b64 s[10:11], s[10:11], s[38:39]
	s_and_b64 vcc, exec, s[10:11]
	s_cbranch_vccnz .LBB0_832
	ds_read_b128 v[38:41], v98
	ds_read_b128 v[100:103], v98 offset:32
	ds_read_b128 v[54:57], v98 offset:4608
	ds_read_b128 v[148:151], v98 offset:4640
	ds_read_b128 v[152:155], v98 offset:64
	ds_read_b128 v[156:159], v98 offset:4672
	ds_read_b128 v[160:163], v98 offset:96
	ds_read_b128 v[164:167], v98 offset:4704
	ds_read_b128 v[168:171], v98 offset:128
	ds_read_b128 v[172:175], v98 offset:4736
	s_cmp_lt_i32 s46, s44
	s_cselect_b64 s[10:11], -1, 0
	s_cmp_gt_u32 s46, s45
	s_cselect_b64 s[38:39], -1, 0
	s_or_b64 s[38:39], s[10:11], s[38:39]
	s_andn2_b64 vcc, exec, s[38:39]
	s_waitcnt lgkmcnt(9)
	v_mfma_f32_32x32x16_bf16 v[38:53], v[38:41], v[82:85], 0
	s_waitcnt lgkmcnt(8)
	v_mfma_f32_32x32x16_bf16 v[38:53], v[100:103], v[78:81], v[38:53]
	s_waitcnt lgkmcnt(7)
	v_mfma_f32_32x32x16_bf16 v[54:69], v[54:57], v[82:85], 0
	s_waitcnt lgkmcnt(6)
	v_mfma_f32_32x32x16_bf16 v[54:69], v[148:151], v[78:81], v[54:69]
	s_waitcnt lgkmcnt(5)
	v_mfma_f32_32x32x16_bf16 v[38:53], v[152:155], v[74:77], v[38:53]
	s_waitcnt lgkmcnt(4)
	v_mfma_f32_32x32x16_bf16 v[54:69], v[156:159], v[74:77], v[54:69]
	s_waitcnt lgkmcnt(3)
	v_mfma_f32_32x32x16_bf16 v[38:53], v[160:163], v[70:73], v[38:53]
	s_waitcnt lgkmcnt(2)
	v_mfma_f32_32x32x16_bf16 v[54:69], v[164:167], v[70:73], v[54:69]
	s_waitcnt lgkmcnt(1)
	v_mfma_f32_32x32x16_bf16 v[38:53], v[168:171], v[86:89], v[38:53]
	s_waitcnt lgkmcnt(0)
	v_mfma_f32_32x32x16_bf16 v[54:69], v[172:175], v[86:89], v[54:69]
	s_cbranch_vccnz .LBB0_836
	v_add_u32_e32 v2, 59, v99
	v_cmp_lt_u32_e32 vcc, s3, v2
	v_add_u32_e32 v2, 27, v99
	s_nop 4
	v_cndmask_b32_e32 v38, v224, v38, vcc
	v_cmp_lt_u32_e32 vcc, s3, v2
	v_add_u32_e32 v2, 58, v99
	s_nop 0
	v_cndmask_b32_e32 v54, v224, v54, vcc
	v_cmp_lt_u32_e32 vcc, s3, v2
	v_add_u32_e32 v2, 26, v99
	s_nop 0
	v_cndmask_b32_e32 v39, v224, v39, vcc
	v_cmp_lt_u32_e32 vcc, s3, v2
	v_add_u32_e32 v2, 57, v99
	s_nop 0
	v_cndmask_b32_e32 v55, v224, v55, vcc
	v_cmp_lt_u32_e32 vcc, s3, v2
	v_add_u32_e32 v2, 25, v99
	s_nop 0
	v_cndmask_b32_e32 v40, v224, v40, vcc
	v_cmp_lt_u32_e32 vcc, s3, v2
	v_add_u32_e32 v2, 56, v99
	s_nop 0
	v_cndmask_b32_e32 v56, v224, v56, vcc
	v_cmp_lt_u32_e32 vcc, s3, v2
	v_add_u32_e32 v2, 24, v99
	s_nop 0
	v_cndmask_b32_e32 v41, v224, v41, vcc
	v_cmp_lt_u32_e32 vcc, s3, v2
	v_add_u32_e32 v2, 51, v99
	s_nop 0
	v_cndmask_b32_e32 v57, v224, v57, vcc
	v_cmp_lt_u32_e32 vcc, s3, v2
	v_add_u32_e32 v2, 19, v99
	s_nop 0
	v_cndmask_b32_e32 v42, v224, v42, vcc
	v_cmp_lt_u32_e32 vcc, s3, v2
	v_add_u32_e32 v2, 50, v99
	s_nop 0
	v_cndmask_b32_e32 v58, v224, v58, vcc
	v_cmp_lt_u32_e32 vcc, s3, v2
	v_add_u32_e32 v2, 18, v99
	s_nop 0
	v_cndmask_b32_e32 v43, v224, v43, vcc
	v_cmp_lt_u32_e32 vcc, s3, v2
	v_add_u32_e32 v2, 49, v99
	s_nop 0
	v_cndmask_b32_e32 v59, v224, v59, vcc
	v_cmp_lt_u32_e32 vcc, s3, v2
	v_add_u32_e32 v2, 17, v99
	s_nop 0
	v_cndmask_b32_e32 v44, v224, v44, vcc
	v_cmp_lt_u32_e32 vcc, s3, v2
	v_add_u32_e32 v2, 48, v99
	s_nop 0
	v_cndmask_b32_e32 v60, v224, v60, vcc
	v_cmp_lt_u32_e32 vcc, s3, v2
	v_add_u32_e32 v2, 16, v99
	s_nop 0
	v_cndmask_b32_e32 v45, v224, v45, vcc
	v_cmp_lt_u32_e32 vcc, s3, v2
	v_add_u32_e32 v2, 43, v99
	s_nop 0
	v_cndmask_b32_e32 v61, v224, v61, vcc
	v_cmp_lt_u32_e32 vcc, s3, v2
	v_add_u32_e32 v2, 11, v99
	s_nop 0
	v_cndmask_b32_e32 v46, v224, v46, vcc
	v_cmp_lt_u32_e32 vcc, s3, v2
	v_add_u32_e32 v2, 42, v99
	s_nop 0
	v_cndmask_b32_e32 v62, v224, v62, vcc
	v_cmp_lt_u32_e32 vcc, s3, v2
	v_add_u32_e32 v2, 10, v99
	s_nop 0
	v_cndmask_b32_e32 v47, v224, v47, vcc
	v_cmp_lt_u32_e32 vcc, s3, v2
	v_add_u32_e32 v2, 41, v99
	s_nop 0
	v_cndmask_b32_e32 v63, v224, v63, vcc
	v_cmp_lt_u32_e32 vcc, s3, v2
	v_add_u32_e32 v2, 9, v99
	s_nop 0
	v_cndmask_b32_e32 v48, v224, v48, vcc
	v_cmp_lt_u32_e32 vcc, s3, v2
	v_add_u32_e32 v2, 40, v99
	s_nop 0
	v_cndmask_b32_e32 v64, v224, v64, vcc
	v_cmp_lt_u32_e32 vcc, s3, v2
	v_add_u32_e32 v2, 8, v99
	s_nop 0
	v_cndmask_b32_e32 v49, v224, v49, vcc
	v_cmp_lt_u32_e32 vcc, s3, v2
	v_add_u32_e32 v2, 35, v99
	s_nop 0
	v_cndmask_b32_e32 v65, v224, v65, vcc
	v_cmp_lt_u32_e32 vcc, s3, v2
	v_add_u32_e32 v2, 3, v99
	s_nop 0
	v_cndmask_b32_e32 v50, v224, v50, vcc
	v_cmp_lt_u32_e32 vcc, s3, v2
	v_add_u32_e32 v2, 34, v99
	s_nop 0
	v_cndmask_b32_e32 v66, v224, v66, vcc
	v_cmp_lt_u32_e32 vcc, s3, v2
	v_add_u32_e32 v2, 2, v99
	s_nop 0
	v_cndmask_b32_e32 v51, v224, v51, vcc
	v_cmp_lt_u32_e32 vcc, s3, v2
	v_add_u32_e32 v2, 33, v99
	s_nop 0
	v_cndmask_b32_e32 v67, v224, v67, vcc
	v_cmp_lt_u32_e32 vcc, s3, v2
	v_add_u32_e32 v2, 1, v99
	s_nop 0
	v_cndmask_b32_e32 v52, v224, v52, vcc
	v_cmp_lt_u32_e32 vcc, s3, v2
	v_add_u32_e32 v2, 32, v99
	s_nop 0
	v_cndmask_b32_e32 v68, v224, v68, vcc
	v_cmp_lt_u32_e32 vcc, s3, v2
	s_nop 1
	v_cndmask_b32_e32 v53, v224, v53, vcc
	v_cmp_lt_u32_e32 vcc, s3, v99
	s_nop 1
	v_cndmask_b32_e32 v69, v224, v69, vcc

.LBB0_854:
	v_add_u32_e32 v131, s39, v125
	ds_read_b128 v[38:41], v131
	ds_read_b128 v[142:145], v131 offset:32
	ds_read_b128 v[54:57], v131 offset:4608
	ds_read_b128 v[148:151], v131 offset:4640
	ds_read_b128 v[152:155], v131 offset:64
	ds_read_b128 v[156:159], v131 offset:4672
	ds_read_b128 v[160:163], v131 offset:96
	ds_read_b128 v[164:167], v131 offset:4704
	ds_read_b128 v[168:171], v131 offset:128
	ds_read_b128 v[172:175], v131 offset:4736
	s_waitcnt lgkmcnt(9)
	v_mfma_f32_32x32x16_bf16 v[38:53], v[38:41], v[82:85], 0
	s_waitcnt lgkmcnt(8)
	v_mfma_f32_32x32x16_bf16 v[38:53], v[142:145], v[78:81], v[38:53]
	s_waitcnt lgkmcnt(7)
	v_mfma_f32_32x32x16_bf16 v[54:69], v[54:57], v[82:85], 0
	s_waitcnt lgkmcnt(6)
	v_mfma_f32_32x32x16_bf16 v[54:69], v[148:151], v[78:81], v[54:69]
	s_waitcnt lgkmcnt(5)
	v_mfma_f32_32x32x16_bf16 v[38:53], v[152:155], v[74:77], v[38:53]
	s_waitcnt lgkmcnt(4)
	v_mfma_f32_32x32x16_bf16 v[54:69], v[156:159], v[74:77], v[54:69]
	s_waitcnt lgkmcnt(3)
	v_mfma_f32_32x32x16_bf16 v[38:53], v[160:163], v[70:73], v[38:53]
	s_waitcnt lgkmcnt(2)
	v_mfma_f32_32x32x16_bf16 v[54:69], v[164:167], v[70:73], v[54:69]
	s_waitcnt lgkmcnt(1)
	v_mfma_f32_32x32x16_bf16 v[38:53], v[168:171], v[86:89], v[38:53]
	s_waitcnt lgkmcnt(0)
	v_mfma_f32_32x32x16_bf16 v[54:69], v[172:175], v[86:89], v[54:69]
	s_nop 11
	v_max_i32_e32 v2, v38, v54
	v_max3_i32 v2, v2, v39, v55
	v_max3_i32 v2, v2, v40, v56
	v_max3_i32 v2, v2, v41, v57
	v_max3_i32 v2, v2, v42, v58
	v_max3_i32 v2, v2, v43, v59
	v_max3_i32 v2, v2, v44, v60
	v_max3_i32 v2, v2, v45, v61
	v_max3_i32 v2, v2, v46, v62
	v_max3_i32 v2, v2, v47, v63
	v_max3_i32 v2, v2, v48, v64
	v_max3_i32 v2, v2, v49, v65
	v_max3_i32 v2, v2, v50, v66
	v_max3_i32 v2, v2, v51, v67
	v_max3_i32 v2, v2, v52, v68
	v_max3_i32 v2, v2, v53, v69
	v_mov_b32_e32 v5, v2
	s_nop 1
	v_permlane32_swap_b32_e32 v2, v5
	v_max_i32_e32 v2, v2, v5
	v_cmp_lt_f32_e32 vcc, s29, v2
	s_cbranch_vccz .LBB0_853
	v_mov_b32_e32 v142, v4
	s_and_saveexec_b64 s[10:11], vcc
	s_cbranch_execz .LBB0_852
	v_add_f32_e32 v2, v4, v2
	v_cvt_pk_bf16_f32 v2, v2, 0
	v_lshlrev_b32_e32 v142, 16, v2
	s_branch .LBB0_852

.LBB0_877:
	ds_read_b128 v[178:181], v125 offset:9216
	ds_read_b128 v[182:185], v125 offset:9248
	ds_read_b128 v[186:189], v125 offset:13824
	ds_read_b128 v[190:193], v125 offset:13856
	ds_read_b128 v[194:197], v125 offset:9280
	ds_read_b128 v[198:201], v125 offset:13888
	ds_read_b128 v[202:205], v125 offset:9312
	ds_read_b128 v[206:209], v125 offset:13920
	v_exp_f32_e32 v4, v38
	v_exp_f32_e32 v5, v39
	v_exp_f32_e32 v38, v54
	v_exp_f32_e32 v39, v55
	v_exp_f32_e32 v40, v40
	v_exp_f32_e32 v41, v41
	v_exp_f32_e32 v54, v56
	v_exp_f32_e32 v55, v57
	v_exp_f32_e32 v42, v42
	v_exp_f32_e32 v56, v58
	v_exp_f32_e32 v43, v43
	v_exp_f32_e32 v57, v59
	v_exp_f32_e32 v58, v60
	v_exp_f32_e32 v59, v61
	v_exp_f32_e32 v60, v62
	v_exp_f32_e32 v61, v63
	v_exp_f32_e32 v62, v64
	v_exp_f32_e32 v63, v65
	v_exp_f32_e32 v64, v50
	v_exp_f32_e32 v65, v51
	v_pk_add_f32 v[50:51], v[126:127], v[4:5]
	v_exp_f32_e32 v44, v44
	v_pk_add_f32 v[50:51], v[38:39], v[50:51]
	v_exp_f32_e32 v45, v45
	v_pk_add_f32 v[50:51], v[40:41], v[50:51]
	v_exp_f32_e32 v46, v46
	v_pk_add_f32 v[50:51], v[54:55], v[50:51]
	v_exp_f32_e32 v47, v47
	v_pk_add_f32 v[50:51], v[42:43], v[50:51]
	v_exp_f32_e32 v48, v48
	v_pk_add_f32 v[50:51], v[56:57], v[50:51]
	v_exp_f32_e32 v49, v49
	v_pk_add_f32 v[50:51], v[44:45], v[50:51]
	v_exp_f32_e32 v66, v66
	v_pk_add_f32 v[50:51], v[58:59], v[50:51]
	v_exp_f32_e32 v67, v67
	v_pk_add_f32 v[50:51], v[46:47], v[50:51]
	v_exp_f32_e32 v70, v52
	v_pk_add_f32 v[50:51], v[60:61], v[50:51]
	v_exp_f32_e32 v71, v53
	v_pk_add_f32 v[50:51], v[48:49], v[50:51]
	v_exp_f32_e32 v68, v68
	v_exp_f32_e32 v69, v69
	v_pk_add_f32 v[50:51], v[62:63], v[50:51]
	v_cvt_pk_bf16_f32 v52, v42, v43
	v_pk_add_f32 v[50:51], v[64:65], v[50:51]
	v_cvt_pk_bf16_f32 v53, v44, v45
	v_cvt_pk_bf16_f32 v42, v38, v39
	v_cvt_pk_bf16_f32 v43, v54, v55
	v_cvt_pk_bf16_f32 v44, v56, v57
	v_cvt_pk_bf16_f32 v45, v58, v59
	v_cvt_pk_bf16_f32 v38, v60, v61
	v_pk_add_f32 v[50:51], v[66:67], v[50:51]
	v_cvt_pk_bf16_f32 v46, v46, v47
	v_pk_add_f32 v[50:51], v[70:71], v[50:51]
	v_cvt_pk_bf16_f32 v47, v48, v49
	v_pk_add_f32 v[126:127], v[68:69], v[50:51]
	v_cvt_pk_bf16_f32 v50, v4, v5
	v_cvt_pk_bf16_f32 v51, v40, v41
	v_cvt_pk_bf16_f32 v48, v64, v65
	v_cvt_pk_bf16_f32 v49, v70, v71
	s_waitcnt lgkmcnt(0)
	v_mfma_f32_32x32x16_bf16 v[6:21], v[178:181], v[50:53], v[6:21]
	v_cvt_pk_bf16_f32 v39, v62, v63
	v_cvt_pk_bf16_f32 v40, v66, v67
	v_cvt_pk_bf16_f32 v41, v68, v69
	v_mfma_f32_32x32x16_bf16 v[22:37], v[186:189], v[50:53], v[22:37]
	v_mfma_f32_32x32x16_bf16 v[6:21], v[182:185], v[46:49], v[6:21]
	v_mfma_f32_32x32x16_bf16 v[22:37], v[190:193], v[46:49], v[22:37]
	v_mfma_f32_32x32x16_bf16 v[6:21], v[194:197], v[42:45], v[6:21]
	v_mfma_f32_32x32x16_bf16 v[22:37], v[198:201], v[42:45], v[22:37]
	v_mfma_f32_32x32x16_bf16 v[6:21], v[202:205], v[38:41], v[6:21]
	v_mfma_f32_32x32x16_bf16 v[22:37], v[206:209], v[38:41], v[22:37]
